# baseline (speedup 1.0000x reference)
_Z8gemm2b_kILi2EEvPKtS1_ii7EpiArgs:
	s_load_dwordx4 s[4:7], s[0:1], 0x0
	s_load_dwordx2 s[12:13], s[0:1], 0x10
	s_load_dwordx4 s[72:75], s[0:1], 0x18
	s_load_dwordx4 s[76:79], s[0:1], 0x38
	s_lshl_b32 s3, s2, 3
	s_and_b32 s3, s3, 56
	s_lshr_b32 s8, s2, 3
	s_and_b32 s9, s8, 3
	s_bfe_u32 s10, s8, 0x10005
	s_lshl_b32 s10, s10, 2
	s_or_b32 s9, s9, s10
	s_or_b32 s3, s3, s9
	s_lshl_b32 s17, s3, 7
	v_readfirstlane_b32 s19, v0
	s_waitcnt lgkmcnt(0)
	s_mul_hi_i32 s9, s13, s17
	s_mul_i32 s8, s13, s17
	s_lshr_b32 s14, s19, 6
	s_lshr_b32 s87, s2, 3
	s_bfe_u32 s88, s87, 0x30002
	s_bfe_u32 s89, s87, 0x10006
	s_lshl_b32 s89, s89, 3
	s_or_b32 s2, s88, s89
	s_bfe_u32 s88, s87, 0x10005
	s_xor_b32 s2, s2, s88
	s_ashr_i32 s11, s13, 31
	s_lshl_b64 s[8:9], s[8:9], 1
	s_mulk_i32 s2, 0xc0
	s_add_u32 s4, s4, s8
	s_addc_u32 s5, s5, s9
	s_mul_hi_i32 s9, s13, s2
	s_mul_i32 s8, s13, s2
	s_ashr_i32 s3, s2, 31
	s_lshl_b64 s[8:9], s[8:9], 1
	s_add_u32 s6, s6, s8
	s_addc_u32 s7, s7, s9
	s_lshr_b32 s8, s19, 1
	v_lshrrev_b32_e32 v1, 4, v0
	s_lshl_b32 s21, s14, 10
	s_and_b32 s16, s8, 0x7fffffc0
	v_xor_b32_e32 v3, v1, v0
	s_bitcmp1_b32 s19, 6
	v_lshrrev_b32_e32 v2, 3, v0
	v_lshlrev_b32_e32 v3, 3, v3
	s_cselect_b32 s18, 0x60, 0
	v_and_b32_e32 v186, 0x7f, v0
	v_add_u32_e32 v186, s17, v186
	v_mov_b32_e32 v187, 0
	v_lshlrev_b64 v[186:187], 5, v[186:187]
	v_lshl_add_u64 v[186:187], s[74:75], 0, v[186:187]
	global_load_dwordx4 v[188:191], v[186:187], off
	global_load_dwordx4 v[192:195], v[186:187], off offset:16
	v_lshrrev_b32_e32 v186, 2, v0
	v_and_or_b32 v186, v186, 12, s18
	v_lshlrev_b32_e32 v186, 2, v186
	s_lshl_b32 s80, s2, 2
	s_add_u32 s82, s76, s80
	s_addc_u32 s83, s77, 0
	s_add_u32 s84, s78, s80
	s_addc_u32 s85, s79, 0
	global_load_dwordx4 v[196:199], v186, s[82:83]
	global_load_dwordx4 v[200:203], v186, s[84:85]
	global_load_dwordx4 v[204:207], v186, s[82:83] offset:64
	global_load_dwordx4 v[208:211], v186, s[84:85] offset:64
	s_cmp_lg_u32 0, -1
	v_mul_lo_u32 v2, s13, v2
	v_and_b32_e32 v3, 56, v3
	s_mov_b32 s10, s13
	s_cselect_b32 s8, 0, 0
	v_add_lshl_u32 v104, v2, v3, 1
	s_add_i32 s22, s21, s8
	s_nop 4
	s_mov_b32 s8, m0
	s_mov_b32 m0, s22
	s_nop 0
	global_load_lds_dwordx4 v104, s[4:5]
	s_mov_b32 m0, s8
	s_lshl_b64 s[14:15], s[10:11], 6
	s_add_u32 s8, s4, s14
	s_addc_u32 s9, s5, s15
	s_add_i32 s23, s22, 0x1000
	s_nop 4
	s_mov_b32 s24, m0
	s_mov_b32 m0, s23
	s_nop 0
	global_load_lds_dwordx4 v104, s[8:9]
	s_mov_b32 m0, s24
	s_add_u32 s8, s8, s14
	s_addc_u32 s9, s9, s15
	s_add_i32 s24, s22, 0x2000
	s_nop 4
	s_mov_b32 s25, m0
	s_mov_b32 m0, s24
	s_nop 0
	global_load_lds_dwordx4 v104, s[8:9]
	s_mov_b32 m0, s25
	s_add_u32 s8, s8, s14
	s_addc_u32 s9, s9, s15
	s_add_i32 s25, s22, 0x3000
	s_nop 4
	s_mov_b32 s26, m0
	s_mov_b32 m0, s25
	s_nop 0
	global_load_lds_dwordx4 v104, s[8:9]
	s_mov_b32 m0, s26
	s_add_i32 s26, s22, 0x4000
	s_nop 4
	s_mov_b32 s8, m0
	s_mov_b32 m0, s26
	s_nop 0
	global_load_lds_dwordx4 v104, s[6:7]
	s_mov_b32 m0, s8
	s_add_u32 s8, s6, s14
	s_addc_u32 s9, s7, s15
	s_add_i32 s27, s22, 0x5000
	s_nop 4
	s_mov_b32 s28, m0
	s_mov_b32 m0, s27
	s_nop 0
	global_load_lds_dwordx4 v104, s[8:9]
	s_mov_b32 m0, s28
	s_add_u32 s8, s8, s14
	s_addc_u32 s9, s9, s15
	s_add_i32 s28, s22, 0x6000
	s_nop 4
	s_mov_b32 s29, m0
	s_mov_b32 m0, s28
	s_nop 0
	global_load_lds_dwordx4 v104, s[8:9]
	s_mov_b32 m0, s29
	s_add_u32 s8, s8, s14
	s_addc_u32 s9, s9, s15
	s_add_i32 s29, s22, 0x7000
	s_nop 4
	s_mov_b32 s30, m0
	s_mov_b32 m0, s29
	s_nop 0
	global_load_lds_dwordx4 v104, s[8:9]
	s_mov_b32 m0, s30
	s_add_u32 s8, s8, s14
	s_addc_u32 s9, s9, s15
	s_add_i32 s30, s22, 0x8000
	s_nop 4
	s_mov_b32 s31, m0
	s_mov_b32 m0, s30
	s_nop 0
	global_load_lds_dwordx4 v104, s[8:9]
	s_mov_b32 m0, s31
	s_add_u32 s8, s8, s14
	s_addc_u32 s9, s9, s15
	s_add_i32 s31, s22, 0x9000
	s_nop 4
	s_mov_b32 s33, m0
	s_mov_b32 m0, s31
	s_nop 0
	global_load_lds_dwordx4 v104, s[8:9]
	s_mov_b32 m0, s33
	s_ashr_i32 s13, s13, 6
	s_mov_b32 s20, 1
	s_cmp_lt_i32 s13, 1
	s_cbranch_scc1 .LBB2_7
	s_lshl_b64 s[8:9], s[10:11], 5
	s_cmp_lg_u32 0, -1
	s_cselect_b32 s33, 0, 0
	s_add_i32 s34, s33, s21
	s_add_i32 s33, s34, 0xa000
	s_add_i32 s34, s34, 0xe000
	s_lshl_b64 s[8:9], s[8:9], 1
	s_add_u32 s45, s4, s8
	s_addc_u32 s46, s5, s9
	s_add_u32 s43, s45, s14
	s_addc_u32 s44, s46, s15
	s_add_u32 s41, s43, s14
	s_addc_u32 s42, s44, s15
	s_add_u32 s35, s6, s8
	s_addc_u32 s38, s7, s9
	s_add_u32 s39, s35, s14
	s_addc_u32 s40, s38, s15
	s_add_u32 s47, s39, s14
	s_addc_u32 s48, s40, s15
	s_add_u32 s49, s47, s14
	s_addc_u32 s50, s48, s15
	s_add_u32 s51, s49, s14
	s_addc_u32 s52, s50, s15
	s_lshl_b64 s[36:37], s[10:11], 7
	s_sub_u32 s36, 0, s36
	s_subb_u32 s37, 0, s37
	s_add_u32 s61, s41, s36
	s_addc_u32 s62, s42, s37
	s_add_u32 s59, s61, s14
	s_addc_u32 s60, s62, s15
	s_add_u32 s57, s59, s14
	s_addc_u32 s58, s60, s15
	s_lshl_b64 s[10:11], s[10:11], 8
	s_sub_u32 s10, 0, s10
	s_subb_u32 s11, 0, s11
	s_add_u32 s53, s51, s10
	s_addc_u32 s54, s52, s11
	s_add_u32 s55, s53, s14
	s_addc_u32 s56, s54, s15
	s_add_u32 s63, s55, s14
	s_addc_u32 s64, s56, s15
	s_add_u32 s65, s63, s14
	s_addc_u32 s66, s64, s15
	s_add_u32 s67, s65, s14
	s_addc_u32 s68, s66, s15
	s_add_u32 s10, s35, 0x80
	s_addc_u32 s11, s38, 0
	s_add_u32 s14, s39, 0x80
	s_addc_u32 s15, s40, 0
	s_add_u32 s35, s47, 0x80
	s_addc_u32 s36, s48, 0
	s_add_u32 s37, s49, 0x80
	s_addc_u32 s38, s50, 0
	s_add_u32 s39, s51, 0x80
	s_addc_u32 s40, s52, 0
	s_add_u32 s41, s41, 0x80
	s_addc_u32 s42, s42, 0
	s_add_u32 s43, s43, 0x80
	s_addc_u32 s44, s44, 0
	s_add_u32 s45, s45, 0x80
	s_addc_u32 s46, s46, 0
	s_add_u32 s47, s53, 0x100
	s_addc_u32 s48, s54, 0
	s_add_u32 s49, s55, 0x100
	s_addc_u32 s50, s56, 0
	s_add_u32 s51, s63, 0x100
	s_addc_u32 s52, s64, 0
	s_add_u32 s53, s65, 0x100
	s_addc_u32 s54, s66, 0
	s_add_u32 s55, s67, 0x100
	s_addc_u32 s56, s68, 0
	v_and_b32_e32 v2, 15, v0
	v_bfe_u32 v0, v0, 1, 3
	s_add_u32 s57, s57, 0x100
	v_bitop3_b32 v0, v1, v0, 3 bitop3:0x6c
	s_addc_u32 s58, s58, 0
	v_lshlrev_b32_e32 v105, 4, v0
	v_or_b32_e32 v0, s18, v2
	s_add_u32 s59, s59, 0x100
	v_xor_b32_e32 v106, 64, v105
	v_lshl_add_u32 v0, v0, 7, 0
	s_addc_u32 s60, s60, 0
	v_or_b32_e32 v1, s16, v2
	v_add_u32_e32 v107, v0, v105
	v_add_u32_e32 v109, v0, v106
	s_add_u32 s61, s61, 0x100
	v_mov_b32_e32 v36, 0
	v_lshl_add_u32 v108, v1, 7, 0
	s_mov_b64 s[8:9], 0
	s_addc_u32 s62, s62, 0
	v_mov_b32_e32 v37, v36
	v_mov_b32_e32 v38, v36
	v_mov_b32_e32 v39, v36
	v_mov_b32_e32 v56, v36
	v_mov_b32_e32 v57, v36
	v_mov_b32_e32 v58, v36
	v_mov_b32_e32 v59, v36
	v_mov_b32_e32 v76, v36
	v_mov_b32_e32 v77, v36
	v_mov_b32_e32 v78, v36
	v_mov_b32_e32 v79, v36
	v_mov_b32_e32 v92, v36
	v_mov_b32_e32 v93, v36
	v_mov_b32_e32 v94, v36
	v_mov_b32_e32 v95, v36
	v_mov_b32_e32 v8, v36
	v_mov_b32_e32 v9, v36
	v_mov_b32_e32 v10, v36
	v_mov_b32_e32 v11, v36
	v_mov_b32_e32 v24, v36
	v_mov_b32_e32 v25, v36
	v_mov_b32_e32 v26, v36
	v_mov_b32_e32 v27, v36
	v_mov_b32_e32 v40, v36
	v_mov_b32_e32 v41, v36
	v_mov_b32_e32 v42, v36
	v_mov_b32_e32 v43, v36
	v_mov_b32_e32 v64, v36
	v_mov_b32_e32 v65, v36
	v_mov_b32_e32 v66, v36
	v_mov_b32_e32 v67, v36
	v_mov_b32_e32 v80, v36
	v_mov_b32_e32 v81, v36
	v_mov_b32_e32 v82, v36
	v_mov_b32_e32 v83, v36
	v_mov_b32_e32 v96, v36
	v_mov_b32_e32 v97, v36
	v_mov_b32_e32 v98, v36
	v_mov_b32_e32 v99, v36
	v_mov_b32_e32 v12, v36
	v_mov_b32_e32 v13, v36
	v_mov_b32_e32 v14, v36
	v_mov_b32_e32 v15, v36
	v_mov_b32_e32 v28, v36
	v_mov_b32_e32 v29, v36
	v_mov_b32_e32 v30, v36
	v_mov_b32_e32 v31, v36
	v_mov_b32_e32 v48, v36
	v_mov_b32_e32 v49, v36
	v_mov_b32_e32 v50, v36
	v_mov_b32_e32 v51, v36
	v_mov_b32_e32 v68, v36
	v_mov_b32_e32 v69, v36
	v_mov_b32_e32 v70, v36
	v_mov_b32_e32 v71, v36
	v_mov_b32_e32 v84, v36
	v_mov_b32_e32 v85, v36
	v_mov_b32_e32 v86, v36
	v_mov_b32_e32 v87, v36
	v_mov_b32_e32 v100, v36
	v_mov_b32_e32 v101, v36
	v_mov_b32_e32 v102, v36
	v_mov_b32_e32 v103, v36
	v_mov_b32_e32 v20, v36
	v_mov_b32_e32 v21, v36
	v_mov_b32_e32 v22, v36
	v_mov_b32_e32 v23, v36
	v_mov_b32_e32 v4, v36
	v_mov_b32_e32 v5, v36
	v_mov_b32_e32 v6, v36
	v_mov_b32_e32 v7, v36
	v_mov_b32_e32 v88, v36
	v_mov_b32_e32 v89, v36
	v_mov_b32_e32 v90, v36
	v_mov_b32_e32 v91, v36
	v_mov_b32_e32 v72, v36
	v_mov_b32_e32 v73, v36
	v_mov_b32_e32 v74, v36
	v_mov_b32_e32 v75, v36
	v_mov_b32_e32 v52, v36
	v_mov_b32_e32 v53, v36
	v_mov_b32_e32 v54, v36
	v_mov_b32_e32 v55, v36
	v_mov_b32_e32 v32, v36
	v_mov_b32_e32 v33, v36
	v_mov_b32_e32 v34, v36
	v_mov_b32_e32 v35, v36
	v_mov_b32_e32 v16, v36
	v_mov_b32_e32 v17, v36
	v_mov_b32_e32 v18, v36
	v_mov_b32_e32 v19, v36
	v_mov_b32_e32 v0, v36
	v_mov_b32_e32 v1, v36
	v_mov_b32_e32 v2, v36
	v_mov_b32_e32 v3, v36
	v_add_u32_e32 v110, 0x4000, v107
	v_add_u32_e32 v111, 0x4000, v109
	s_branch .LBB2_3
